# C3 item loop: V^T/q loads requested with the attention-norm inputs; epilogue gain/gate loads requested during the last direction step
# speedup vs baseline: 1.0093x; 1.0093x over previous
; __device__ __forceinline__ float kf(float x) { asm volatile("" : "+s"(x)); return x; }
; __device__ __forceinline__ void c3_phase(LAS unsigned char* lds, const bf16_t* __restrict__ QH, const bf16_t* __restrict__ LF, const bf16_t* __restrict__ VTH, const bf16_t* __restrict__ SIN, ...
;     ...
;     for (int item = c; item < NB * 4 * 32; item += G) {
;         const int b = item >> 7, h = (item >> 5) & 3, j = item & 31;
;         const size_t tok0 = (size_t)b * SEQ + j * 64;
;         { const int t = tid >> 3, c16 = (tid & 7) * 16; const size_t tok = tok0 + t;
;           const f32x4 s0 = *(const f32x4*)(SSQ + tok * 8), s1 = *(const f32x4*)(SSQ + tok * 8 + 4);
;           const float r = rsqrtf(((s0[0] + s0[1]) + (s0[2] + s0[3]) + (s1[0] + s1[1]) + (s1[2] + s1[3])) * (1.f / 512) + kf(EPS));
; #pragma unroll
;           for (int k = 0; k < 2; ++k) {
;               const u32x4 a = *(const u32x4*)(AO + tok * 512 + h * 128 + c16 + k * 8);
;               const f32x4 g0 = *(const f32x4*)(attn_gain + h * 128 + c16 + k * 8), g1 = *(const f32x4*)(attn_gain + h * 128 + c16 + k * 8 + 4);
;               u32x4 o;
;               o.x = cvt_pk_bf16(__uint_as_float(a.x << 16) * r * g0[0], __uint_as_float(a.x & 0xffff0000u) * r * g0[1]);
;     ...
;         float ss = 0.f;
; #pragma unroll
;         for (int et = 0; et < 4; ++et) ss += o[et][0] * o[et][0] + o[et][1] * o[et][1] + o[et][2] * o[et][2] + o[et][3] * o[et][3];
;         ss += shx(ss, 16); ss += shx(ss, 32);
;         if (g4 == 0) red[wid * 16 + l15] = ss;
;         __syncthreads();
;         const float tot = red[wid * 16 + l15] + red[(wid ^ 4) * 16 + l15];
;         const float rr = rsqrtf(tot * (1.f / 128) + kf(EPS));
;         const size_t tok = tok0 + tau * 16 + l15;
; #pragma unroll
;         for (int et = 0; et < 4; ++et) {
;             const int e0 = (eh * 4 + et) * 16 + 4 * g4;
;             const f32x4 gn = *(const f32x4*)(hg_gain + e0);
;             const u32x2 gv = *(const u32x2*)(GS + tok * 512 + h * 128 + e0);
;             u32x2 w;
;             w.x = cvt_pk_bf16(o[et][0] * rr * gn[0] * __uint_as_float(gv.x << 16), o[et][1] * rr * gn[1] * __uint_as_float(gv.x & 0xffff0000u));
;             w.y = cvt_pk_bf16(o[et][2] * rr * gn[2] * __uint_as_float(gv.y << 16), o[et][3] * rr * gn[3] * __uint_as_float(gv.y & 0xffff0000u));
;             *(u32x2*)(MIX + tok * D + 512 + h * 128 + e0) = w;
;         }
.LBB0_1094:
	s_or_b64 exec, exec, s[2:3]
	v_readlane_b32 s78, v254, 28
	v_readlane_b32 s79, v254, 29
	v_readlane_b32 s3, v254, 27
	v_or_b32_e32 v82, s78, v64
	v_mov_b32_e32 v83, s79
	v_readlane_b32 s78, v254, 14
	v_lshlrev_b64 v[40:41], 10, v[82:83]
	v_readlane_b32 s79, v254, 15
	s_mov_b32 s91, s81
	s_lshl_b32 s90, s3, 1
	v_lshl_add_u64 v[48:49], s[78:79], 0, v[40:41]
	s_mov_b32 s2, 0x358637bd
	v_lshl_add_u64 v[84:85], v[48:49], 0, s[90:91]
	s_waitcnt lgkmcnt(0)
	s_barrier
	ds_read_b32 v92, v178
	ds_read_b32 v93, v177
	v_lshl_add_u64 v[84:85], v[84:85], 0, v[80:81]
	v_mov_b32_e32 v94, s2
	s_waitcnt lgkmcnt(0)
	v_add_f32_e32 v92, v92, v93
	v_fmac_f32_e32 v94, 0x3c000000, v92
	s_mov_b32 s2, 0x800000
	v_mul_f32_e32 v92, 0x4b800000, v94
	v_cmp_gt_f32_e64 s[80:81], s2, v94
	v_readlane_b32 s86, v254, 25
	v_lshlrev_b64 v[82:83], 11, v[82:83]
	v_cndmask_b32_e64 v92, v94, v92, s[80:81]
	v_rsq_f32_e32 v92, v92
	v_readlane_b32 s87, v254, 26
	v_readlane_b32 s2, v254, 30
	v_readlane_b32 s3, v254, 31
	v_mul_f32_e32 v93, 0x45800000, v92
	v_cndmask_b32_e64 v92, v92, v93, s[80:81]
	v_pk_mul_f32 v[18:19], v[18:19], v[92:93] op_sel_hi:[1,0]
	v_pk_mul_f32 v[20:21], v[20:21], v[92:93] op_sel_hi:[1,0]
	v_lshl_add_u64 v[82:83], s[86:87], 0, v[82:83]
	v_pk_mul_f32 v[26:27], v[26:27], v[92:93] op_sel_hi:[1,0]
	v_pk_mul_f32 v[28:29], v[28:29], v[92:93] op_sel_hi:[1,0]
	v_pk_mul_f32 v[22:23], v[22:23], v[92:93] op_sel_hi:[1,0]
	v_pk_mul_f32 v[24:25], v[24:25], v[92:93] op_sel_hi:[1,0]
	v_pk_mul_f32 v[30:31], v[30:31], v[92:93] op_sel_hi:[1,0]
	v_pk_mul_f32 v[32:33], v[32:33], v[92:93] op_sel_hi:[1,0]
	v_lshl_add_u64 v[82:83], v[82:83], 0, s[90:91]
	s_andn2_b64 vcc, exec, s[2:3]
	v_lshl_add_u64 v[82:83], v[82:83], 0, v[80:81]
	s_mov_b32 s80, 0x800000
	s_waitcnt vmcnt(7)
	v_pk_mul_f32 v[18:19], v[190:191], v[18:19]
	v_pk_mul_f32 v[20:21], v[192:193], v[20:21]
	s_waitcnt vmcnt(3)
	v_lshlrev_b32_e32 v36, 16, v238
	v_and_b32_e32 v37, 0xffff0000, v238
	v_lshlrev_b32_e32 v38, 16, v239
	v_and_b32_e32 v39, 0xffff0000, v239
	v_pk_mul_f32 v[26:27], v[194:195], v[26:27]
	v_pk_mul_f32 v[28:29], v[196:197], v[28:29]
	v_pk_mul_f32 v[22:23], v[22:23], v[198:199]
	v_pk_mul_f32 v[24:25], v[24:25], v[200:201]
	v_pk_mul_f32 v[30:31], v[30:31], v[202:203]
	v_pk_mul_f32 v[32:33], v[32:33], v[204:205]
	s_waitcnt vmcnt(2)
	v_lshlrev_b32_e32 v40, 16, v240
	v_and_b32_e32 v41, 0xffff0000, v240
	v_lshlrev_b32_e32 v42, 16, v241
	v_and_b32_e32 v43, 0xffff0000, v241
	s_waitcnt vmcnt(1)
	v_lshlrev_b32_e32 v44, 16, v242
	v_and_b32_e32 v45, 0xffff0000, v242
	v_lshlrev_b32_e32 v46, 16, v243
	v_and_b32_e32 v47, 0xffff0000, v243
	s_waitcnt vmcnt(0)
	v_lshlrev_b32_e32 v48, 16, v244
	v_and_b32_e32 v49, 0xffff0000, v244
	v_lshlrev_b32_e32 v50, 16, v245
	v_and_b32_e32 v51, 0xffff0000, v245
	v_pk_mul_f32 v[18:19], v[18:19], v[36:37]
	v_pk_mul_f32 v[20:21], v[20:21], v[38:39]
	v_pk_mul_f32 v[26:27], v[26:27], v[40:41]
	v_pk_mul_f32 v[28:29], v[28:29], v[42:43]
	v_pk_mul_f32 v[22:23], v[22:23], v[44:45]
	v_pk_mul_f32 v[24:25], v[24:25], v[46:47]
	v_pk_mul_f32 v[30:31], v[30:31], v[48:49]
	v_pk_mul_f32 v[32:33], v[32:33], v[50:51]
	v_cvt_pk_bf16_f32 v18, v18, v19
	v_cvt_pk_bf16_f32 v19, v20, v21
	v_cvt_pk_bf16_f32 v20, v26, v27
	v_cvt_pk_bf16_f32 v21, v28, v29
	v_cvt_pk_bf16_f32 v22, v22, v23
	v_cvt_pk_bf16_f32 v23, v24, v25
	v_cvt_pk_bf16_f32 v24, v30, v31
	v_cvt_pk_bf16_f32 v25, v32, v33
	global_store_dwordx2 v[82:83], v[18:19], off offset:1024
	global_store_dwordx2 v[82:83], v[20:21], off offset:1056
	global_store_dwordx2 v[82:83], v[22:23], off offset:1088
	global_store_dwordx2 v[82:83], v[24:25], off offset:1120
	s_cbranch_vccz .LBB0_1113
.LBB0_1095:
	s_ashr_i32 s2, s82, 7
	s_and_b32 s78, s82, 31
	s_ashr_i32 s3, s2, 31
	s_mov_b32 s89, s82
	s_lshl_b64 s[82:83], s[2:3], 11
	s_lshl_b32 s79, s78, 6
	s_or_b32 s82, s82, s79
	v_lshl_add_u64 v[82:83], s[82:83], 0, v[54:55]
	v_readlane_b32 s84, v254, 18
	v_lshlrev_b64 v[18:19], 5, v[82:83]
	v_readlane_b32 s85, v254, 19
	s_mov_b64 s[80:81], s[86:87]
	v_readlane_b32 s86, v254, 16
	v_lshl_add_u64 v[22:23], s[84:85], 0, v[18:19]
	global_load_dwordx4 v[18:21], v[22:23], off offset:16
	s_nop 0
	global_load_dwordx4 v[22:25], v[22:23], off
	s_bfe_u32 s79, s89, 0x20005
	v_lshlrev_b64 v[26:27], 10, v[82:83]
	v_readlane_b32 s87, v254, 17
	s_lshl_b32 s90, s79, 8
	s_mov_b32 s84, 0x358637bd
	v_lshl_add_u64 v[26:27], s[86:87], 0, v[26:27]
	v_lshl_add_u64 v[26:27], v[26:27], 0, s[90:91]
	v_lshl_add_u64 v[30:31], v[26:27], 0, v[34:35]
	global_load_dwordx4 v[26:29], v[30:31], off
	s_nop 0
	global_load_dwordx4 v[30:33], v[30:31], off offset:16
	s_mov_b32 s87, s91
	s_lshl_b32 s86, s79, 9
	v_lshl_add_u64 v[48:49], v[56:57], 0, s[86:87]
	global_load_dwordx4 v[36:39], v[48:49], off
	global_load_dwordx4 v[40:43], v[48:49], off offset:16
	global_load_dwordx4 v[44:47], v[48:49], off offset:32
	s_nop 0
	global_load_dwordx4 v[48:51], v[48:49], off offset:48
	v_mov_b32_e32 v90, s84
	s_mov_b32 s85, 0x800000
	s_lshl_b32 vcc_lo, s79, 7
	s_lshl_b64 s[92:93], s[2:3], 9
	v_writelane_b32 v254, vcc_lo, 27
	s_or_b32 s92, s92, vcc_lo
	v_lshlrev_b64 v[82:83], 11, v[82:83]
	v_lshl_add_u64 v[82:83], s[80:81], 0, v[82:83]
	v_lshl_add_u64 v[82:83], v[82:83], 0, s[90:91]
	v_lshl_add_u64 v[82:83], v[82:83], 0, v[34:35]
	s_lshl_b32 s86, s78, 7
	v_lshl_add_u64 v[86:87], s[92:93], 0, v[54:55]
	v_writelane_b32 v254, s82, 28
	v_lshl_add_u64 v[84:85], v[58:59], 0, s[86:87]
	v_lshlrev_b64 v[86:87], 12, v[86:87]
	v_lshl_add_u64 v[86:87], v[84:85], 0, v[86:87]
	v_writelane_b32 v254, s83, 29
	v_lshl_add_u64 v[230:231], s[92:93], 0, v[70:71]
	v_lshlrev_b64 v[230:231], 12, v[230:231]
	v_lshl_add_u64 v[230:231], v[84:85], 0, v[230:231]
	global_load_dwordx4 v[222:225], v[86:87], off
	global_load_dwordx4 v[226:229], v[230:231], off
	v_lshl_add_u64 v[232:233], s[82:83], 0, v[52:53]
	v_lshlrev_b64 v[232:233], 10, v[232:233]
	v_lshl_add_u64 v[234:235], v[60:61], 0, s[90:91]
	v_lshl_add_u64 v[232:233], v[234:235], 0, v[232:233]
	v_mov_b32_e32 v236, 0x2000
	v_mov_b32_e32 v237, 0
	global_load_ushort v190, v[232:233], off
	global_load_ushort v191, v[232:233], off offset:1024
	global_load_ushort v192, v[232:233], off offset:2048
	global_load_ushort v193, v[232:233], off offset:3072
	v_lshl_add_u64 v[232:233], v[232:233], 0, v[236:237]
	global_load_ushort v194, v[232:233], off offset:-4096
	global_load_ushort v195, v[232:233], off offset:-3072
	global_load_ushort v196, v[232:233], off offset:-2048
	global_load_ushort v197, v[232:233], off offset:-1024
	global_load_ushort v198, v[232:233], off
	global_load_ushort v199, v[232:233], off offset:1024
	global_load_ushort v200, v[232:233], off offset:2048
	global_load_ushort v201, v[232:233], off offset:3072
	v_lshl_add_u64 v[232:233], v[232:233], 0, v[236:237]
	global_load_ushort v202, v[232:233], off offset:-4096
	global_load_ushort v203, v[232:233], off offset:-3072
	global_load_ushort v204, v[232:233], off offset:-2048
	global_load_ushort v205, v[232:233], off offset:-1024
	s_waitcnt vmcnt(24)
; #define LAS __attribute__((address_space(3)))
; __device__ __forceinline__ unsigned cvt_pk_bf16(float lo, float hi) { const bf16x2_t r = __builtin_convertvector((f32x2_t){lo, hi}, bf16x2_t); return __builtin_bit_cast(unsigned, r); }
; __device__ __forceinline__ float bf2f(bf16_t b) { return __uint_as_float(((unsigned)b) << 16); }
; __device__ __forceinline__ float kf(float x) { asm volatile("" : "+s"(x)); return x; }
; __device__ __forceinline__ void c3_phase(LAS unsigned char* lds, const bf16_t* __restrict__ QH, const bf16_t* __restrict__ LF, const bf16_t* __restrict__ VTH, const bf16_t* __restrict__ SIN, ...
;     ...
;         { const int t = tid >> 3, c16 = (tid & 7) * 16; const size_t tok = tok0 + t;
;           const f32x4 s0 = *(const f32x4*)(SSQ + tok * 8), s1 = *(const f32x4*)(SSQ + tok * 8 + 4);
;           const float r = rsqrtf(((s0[0] + s0[1]) + (s0[2] + s0[3]) + (s1[0] + s1[1]) + (s1[2] + s1[3])) * (1.f / 512) + kf(EPS));
; #pragma unroll
;           for (int k = 0; k < 2; ++k) {
;               const u32x4 a = *(const u32x4*)(AO + tok * 512 + h * 128 + c16 + k * 8);
;               const f32x4 g0 = *(const f32x4*)(attn_gain + h * 128 + c16 + k * 8), g1 = *(const f32x4*)(attn_gain + h * 128 + c16 + k * 8 + 4);
;               u32x4 o;
;               o.x = cvt_pk_bf16(__uint_as_float(a.x << 16) * r * g0[0], __uint_as_float(a.x & 0xffff0000u) * r * g0[1]);
;               o.y = cvt_pk_bf16(__uint_as_float(a.y << 16) * r * g0[2], __uint_as_float(a.y & 0xffff0000u) * r * g0[3]);
;               o.z = cvt_pk_bf16(__uint_as_float(a.z << 16) * r * g1[0], __uint_as_float(a.z & 0xffff0000u) * r * g1[1]);
;               o.w = cvt_pk_bf16(__uint_as_float(a.w << 16) * r * g1[2], __uint_as_float(a.w & 0xffff0000u) * r * g1[3]);
;               *(u32x4*)(MIX + tok * D + h * 128 + c16 + k * 8) = o;
;           } }
;         __syncthreads();
; #pragma unroll
;         for (int i = 0; i < 2; ++i) { const int ch = tid + i * 512, e = ch >> 3, part = ch & 7;
;             *(LAS u32x4*)(lds + C3_VT + e * R144 + part * 16) = *(const u32x4*)(VTH + ((size_t)b * 512 + h * 128 + e) * SEQ + j * 64 + part * 8); }
;         f32x4 o[4];
; #pragma unroll
;         for (int et = 0; et < 4; ++et) o[et] = (f32x4){0.f, 0.f, 0.f, 0.f};
;         float qv[16];
; #pragma unroll
;         for (int i = 0; i < 16; ++i) qv[i] = bf2f(QH[(tok0 + tq * 16 + i) * 512 + h * 128 + d]);
	v_mov_b32_e32 v88, v23
	v_mov_b32_e32 v89, v24
	v_mov_b32_e32 v23, v25
	v_mov_b32_e32 v24, v20
	v_mov_b32_e32 v25, v18
	v_mov_b32_e32 v18, v21
	v_pk_add_f32 v[20:21], v[88:89], v[22:23]
	v_pk_add_f32 v[18:19], v[24:25], v[18:19]
	v_add_f32_e32 v89, v20, v21
	v_add_f32_e32 v19, v89, v19
	v_add_f32_e32 v18, v18, v19
	v_fmac_f32_e32 v90, 0x3b000000, v18
	v_mul_f32_e32 v18, 0x4b800000, v90
	v_cmp_gt_f32_e32 vcc, s85, v90
	s_waitcnt vmcnt(22)
	v_lshlrev_b32_e32 v88, 16, v32
	v_and_b32_e32 v89, 0xffff0000, v32
	v_cndmask_b32_e32 v18, v90, v18, vcc
	v_rsq_f32_e32 v90, v18
	v_lshlrev_b32_e32 v20, 16, v26
	v_and_b32_e32 v21, 0xffff0000, v26
	v_lshlrev_b32_e32 v22, 16, v27
	v_mul_f32_e32 v32, 0x45800000, v90
	v_and_b32_e32 v23, 0xffff0000, v27
	v_lshlrev_b32_e32 v24, 16, v28
	v_and_b32_e32 v25, 0xffff0000, v28
	v_lshlrev_b32_e32 v26, 16, v29
	v_and_b32_e32 v27, 0xffff0000, v29
	v_cndmask_b32_e32 v32, v90, v32, vcc
	v_lshlrev_b32_e32 v28, 16, v30
	v_and_b32_e32 v29, 0xffff0000, v30
	v_lshlrev_b32_e32 v30, 16, v31
	v_and_b32_e32 v31, 0xffff0000, v31
	v_lshlrev_b32_e32 v18, 16, v33
	v_and_b32_e32 v19, 0xffff0000, v33
	v_pk_mul_f32 v[20:21], v[32:33], v[20:21] op_sel_hi:[0,1]
	v_pk_mul_f32 v[22:23], v[32:33], v[22:23] op_sel_hi:[0,1]
	v_pk_mul_f32 v[24:25], v[32:33], v[24:25] op_sel_hi:[0,1]
	v_pk_mul_f32 v[26:27], v[32:33], v[26:27] op_sel_hi:[0,1]
	v_pk_mul_f32 v[28:29], v[32:33], v[28:29] op_sel_hi:[0,1]
	v_pk_mul_f32 v[30:31], v[32:33], v[30:31] op_sel_hi:[0,1]
	v_pk_mul_f32 v[88:89], v[32:33], v[88:89] op_sel_hi:[0,1]
	v_pk_mul_f32 v[18:19], v[32:33], v[18:19] op_sel_hi:[0,1]
	s_waitcnt vmcnt(21)
	v_pk_mul_f32 v[20:21], v[36:37], v[20:21]
	v_pk_mul_f32 v[22:23], v[38:39], v[22:23]
	s_waitcnt vmcnt(20)
	v_pk_mul_f32 v[24:25], v[40:41], v[24:25]
	v_pk_mul_f32 v[26:27], v[42:43], v[26:27]
	s_waitcnt vmcnt(19)
	v_pk_mul_f32 v[28:29], v[44:45], v[28:29]
	v_pk_mul_f32 v[30:31], v[46:47], v[30:31]
	s_waitcnt vmcnt(18)
	v_pk_mul_f32 v[32:33], v[48:49], v[88:89]
	v_pk_mul_f32 v[36:37], v[50:51], v[18:19]
	v_cvt_pk_bf16_f32 v18, v20, v21
	v_cvt_pk_bf16_f32 v19, v22, v23
	v_cvt_pk_bf16_f32 v20, v24, v25
	v_cvt_pk_bf16_f32 v21, v26, v27
	v_cvt_pk_bf16_f32 v22, v28, v29
	v_cvt_pk_bf16_f32 v23, v30, v31
	v_cvt_pk_bf16_f32 v24, v32, v33
	v_cvt_pk_bf16_f32 v25, v36, v37
	global_store_dwordx4 v[82:83], v[18:21], off
	global_store_dwordx4 v[82:83], v[22:25], off offset:16
	v_lshl_add_u64 v[26:27], s[82:83], 0, v[52:53]
	v_lshl_add_u64 v[18:19], s[92:93], 0, v[70:71]
	v_lshlrev_b64 v[18:19], 12, v[18:19]
	v_or_b32_e32 v38, 2, v26
	v_mov_b32_e32 v39, v27
	v_or_b32_e32 v46, 4, v26
	v_mov_b32_e32 v47, v27
	v_lshl_add_u64 v[22:23], v[84:85], 0, v[18:19]
	v_lshl_add_u64 v[28:29], v[60:61], 0, s[90:91]
	v_lshlrev_b64 v[30:31], 10, v[26:27]
	v_or_b32_e32 v32, 1, v26
	v_mov_b32_e32 v33, v27
	v_lshlrev_b64 v[40:41], 10, v[38:39]
	v_or_b32_e32 v42, 3, v26
	v_mov_b32_e32 v43, v27
	v_lshlrev_b64 v[48:49], 10, v[46:47]
	v_or_b32_e32 v50, 5, v26
	v_mov_b32_e32 v51, v27
	v_or_b32_e32 v132, 6, v26
	v_mov_b32_e32 v133, v27
	v_or_b32_e32 v134, 7, v26
	v_mov_b32_e32 v135, v27
	s_barrier
	v_lshl_add_u64 v[30:31], v[28:29], 0, v[30:31]
	v_lshlrev_b64 v[36:37], 10, v[32:33]
	v_lshl_add_u64 v[40:41], v[28:29], 0, v[40:41]
	v_lshlrev_b64 v[44:45], 10, v[42:43]
	v_lshl_add_u64 v[48:49], v[28:29], 0, v[48:49]
	v_lshlrev_b64 v[82:83], 10, v[50:51]
	v_lshlrev_b64 v[84:85], 10, v[132:133]
	v_lshlrev_b64 v[86:87], 10, v[134:135]
	v_lshl_add_u64 v[36:37], v[28:29], 0, v[36:37]
	v_lshl_add_u64 v[44:45], v[28:29], 0, v[44:45]
	v_lshl_add_u64 v[82:83], v[28:29], 0, v[82:83]
	v_lshl_add_u64 v[84:85], v[28:29], 0, v[84:85]
	v_lshl_add_u64 v[86:87], v[28:29], 0, v[86:87]
	v_or_b32_e32 v30, 8, v26
	v_mov_b32_e32 v31, v27
	v_or_b32_e32 v40, 9, v26
	v_mov_b32_e32 v41, v27
	v_or_b32_e32 v48, 10, v26
	v_mov_b32_e32 v49, v27
	v_or_b32_e32 v142, 11, v26
	v_mov_b32_e32 v143, v27
	v_or_b32_e32 v144, 12, v26
	v_mov_b32_e32 v145, v27
	v_or_b32_e32 v146, 13, v26
	v_mov_b32_e32 v147, v27
	v_or_b32_e32 v148, 14, v26
	v_mov_b32_e32 v149, v27
	v_or_b32_e32 v150, 15, v26
	v_mov_b32_e32 v151, v27
	v_lshlrev_b64 v[36:37], 10, v[30:31]
	v_lshlrev_b64 v[44:45], 10, v[40:41]
	v_lshlrev_b64 v[82:83], 10, v[48:49]
	v_lshlrev_b64 v[84:85], 10, v[142:143]
	v_lshlrev_b64 v[86:87], 10, v[144:145]
	v_lshlrev_b64 v[88:89], 10, v[146:147]
	v_lshlrev_b64 v[90:91], 10, v[148:149]
	v_lshlrev_b64 v[92:93], 10, v[150:151]
	v_lshl_add_u64 v[36:37], v[28:29], 0, v[36:37]
	v_lshl_add_u64 v[44:45], v[28:29], 0, v[44:45]
	v_lshl_add_u64 v[82:83], v[28:29], 0, v[82:83]
	v_lshl_add_u64 v[84:85], v[28:29], 0, v[84:85]
	v_lshl_add_u64 v[86:87], v[28:29], 0, v[86:87]
	v_lshl_add_u64 v[88:89], v[28:29], 0, v[88:89]
	v_lshl_add_u64 v[90:91], v[28:29], 0, v[90:91]
	v_lshl_add_u64 v[28:29], v[28:29], 0, v[92:93]
	v_readlane_b32 s80, v254, 20
	s_add_i32 s82, s89, s80
	s_cmpk_lt_i32 s82, 0x400
	s_cselect_b64 s[86:87], -1, 0
	s_cmpk_gt_i32 s82, 0x3ff
	s_cselect_b64 s[80:81], -1, 0
	s_lshl_b64 s[2:3], s[2:3], 7
	s_lshl_b32 s79, s79, 5
	s_or_b32 s2, s2, s79
	s_and_b32 s83, s82, 31
	s_or_b32 s2, s2, s78
	s_ashr_i32 s92, s82, 7
	s_bfe_u32 s89, s82, 0x20005
	s_lshl_b32 vcc_lo, s83, 6
	s_mov_b32 vcc_hi, s91
	s_lshl_b64 s[2:3], s[2:3], 15
	s_waitcnt vmcnt(19)
; #define LAS __attribute__((address_space(3)))
; __device__ __forceinline__ float bf2f(bf16_t b) { return __uint_as_float(((unsigned)b) << 16); }
; #define lds lds_hidden(lds0)
; __device__ __forceinline__ void c3_phase(LAS unsigned char* lds, const bf16_t* __restrict__ QH, const bf16_t* __restrict__ LF, const bf16_t* __restrict__ VTH, const bf16_t* __restrict__ SIN, ...
;     ...
;         for (int i = 0; i < 2; ++i) { const int ch = tid + i * 512, e = ch >> 3, part = ch & 7;
;             *(LAS u32x4*)(lds + C3_VT + e * R144 + part * 16) = *(const u32x4*)(VTH + ((size_t)b * 512 + h * 128 + e) * SEQ + j * 64 + part * 8); }
;         f32x4 o[4];
; #pragma unroll
;         for (int et = 0; et < 4; ++et) o[et] = (f32x4){0.f, 0.f, 0.f, 0.f};
;         float qv[16];
; #pragma unroll
;         for (int i = 0; i < 16; ++i) qv[i] = bf2f(QH[(tok0 + tq * 16 + i) * 512 + h * 128 + d]);
	ds_write_b128 v179, v[222:225] offset:52224
	s_waitcnt vmcnt(18)
	ds_write_b128 v180, v[226:229] offset:52224
	s_ashr_i32 s93, s92, 31
	v_lshl_add_u64 v[18:19], vcc, 0, v[52:53]
	s_lshl_b32 vcc_lo, s89, 8
	v_lshl_add_u64 v[20:21], v[62:63], 0, vcc
	v_lshlrev_b64 v[18:19], 11, v[18:19]
	v_lshl_add_u64 v[24:25], v[62:63], 0, s[90:91]
	s_waitcnt vmcnt(17)
	v_lshlrev_b32_e32 v190, 16, v190
	s_waitcnt vmcnt(16)
	v_lshlrev_b32_e32 v191, 16, v191
	s_waitcnt vmcnt(15)
	v_lshlrev_b32_e32 v192, 16, v192
	s_waitcnt vmcnt(14)
	v_lshlrev_b32_e32 v193, 16, v193
	s_waitcnt vmcnt(13)
	v_lshlrev_b32_e32 v194, 16, v194
	s_waitcnt vmcnt(12)
	v_lshlrev_b32_e32 v195, 16, v195
	v_writelane_b32 v254, s80, 30
	s_waitcnt vmcnt(11)
	v_lshlrev_b32_e32 v196, 16, v196
	s_waitcnt vmcnt(10)
	v_lshlrev_b32_e32 v197, 16, v197
	v_writelane_b32 v254, s81, 31
	s_lshl_b64 s[84:85], s[92:93], 7
	s_lshl_b32 s80, s89, 5
	s_or_b32 s80, s84, s80
	s_or_b32 s84, s80, s83
	s_lshl_b64 s[84:85], s[84:85], 15
	v_lshl_add_u64 v[22:23], v[66:67], 0, s[84:85]
	s_mov_b32 s81, s91
	v_lshl_add_u64 v[112:113], v[22:23], 0, v[72:73]
	v_lshl_add_u64 v[114:115], v[22:23], 0, v[74:75]
	v_lshl_add_u64 v[116:117], v[22:23], 0, v[76:77]
	v_lshl_add_u64 v[118:119], v[22:23], 0, v[78:79]
	s_waitcnt vmcnt(9)
	v_lshlrev_b32_e32 v198, 16, v198
	s_waitcnt vmcnt(8)
	v_lshlrev_b32_e32 v199, 16, v199
	s_waitcnt vmcnt(7)
	v_lshlrev_b32_e32 v200, 16, v200
	s_waitcnt vmcnt(6)
	v_lshlrev_b32_e32 v201, 16, v201
	s_waitcnt vmcnt(5)
	v_lshlrev_b32_e32 v202, 16, v202
	s_waitcnt vmcnt(4)
	v_lshlrev_b32_e32 v203, 16, v203
	s_waitcnt vmcnt(3)
	v_lshlrev_b32_e32 v204, 16, v204
	s_waitcnt vmcnt(2)
	v_lshlrev_b32_e32 v205, 16, v205
	v_lshl_add_u64 v[28:29], v[66:67], 0, s[2:3]
	s_mov_b64 s[2:3], 0x2000000
	v_lshl_add_u64 v[28:29], v[28:29], 0, s[2:3]
	s_lshl_b64 s[2:3], s[92:93], 22
	v_lshl_add_u64 v[20:21], v[20:21], 0, s[2:3]
	v_lshl_add_u64 v[82:83], v[20:21], 0, v[18:19]
	v_lshlrev_b64 v[18:19], 11, v[26:27]
	v_lshl_add_u64 v[120:121], v[24:25], 0, v[18:19]
	v_lshlrev_b64 v[18:19], 11, v[32:33]
	v_lshl_add_u64 v[122:123], v[24:25], 0, v[18:19]
	v_lshlrev_b64 v[18:19], 11, v[38:39]
	s_mov_b64 s[2:3], 0x1000
	v_lshl_add_u64 v[124:125], v[24:25], 0, v[18:19]
	v_lshlrev_b64 v[18:19], 11, v[42:43]
	v_lshl_add_u64 v[84:85], v[82:83], 0, s[2:3]
	s_mov_b64 s[2:3], 0x1800
	v_lshl_add_u64 v[126:127], v[24:25], 0, v[18:19]
	v_lshlrev_b64 v[18:19], 11, v[46:47]
	v_lshl_add_u64 v[86:87], v[82:83], 0, s[2:3]
	s_mov_b64 s[2:3], 0x2000
	v_lshl_add_u64 v[128:129], v[24:25], 0, v[18:19]
	v_lshlrev_b64 v[18:19], 11, v[50:51]
	v_lshl_add_u64 v[88:89], v[82:83], 0, s[2:3]
	s_mov_b64 s[2:3], 0x2800
	v_lshl_add_u64 v[130:131], v[24:25], 0, v[18:19]
	v_lshlrev_b64 v[18:19], 11, v[132:133]
	v_lshl_add_u64 v[90:91], v[82:83], 0, s[2:3]
	s_mov_b64 s[2:3], 0x3000
	v_lshl_add_u64 v[132:133], v[24:25], 0, v[18:19]
	v_lshlrev_b64 v[18:19], 11, v[134:135]
	v_lshl_add_u64 v[92:93], v[82:83], 0, s[2:3]
	s_mov_b64 s[2:3], 0x3800
	v_lshl_add_u64 v[134:135], v[24:25], 0, v[18:19]
	v_lshlrev_b64 v[18:19], 11, v[30:31]
	v_lshl_add_u64 v[94:95], v[82:83], 0, s[2:3]
	s_mov_b64 s[2:3], 0x4000
	v_lshl_add_u64 v[136:137], v[24:25], 0, v[18:19]
	v_lshlrev_b64 v[18:19], 11, v[40:41]
	v_lshl_add_u64 v[96:97], v[82:83], 0, s[2:3]
	s_mov_b64 s[2:3], 0x4800
	v_lshl_add_u64 v[138:139], v[24:25], 0, v[18:19]
	v_lshlrev_b64 v[18:19], 11, v[48:49]
	v_lshl_add_u64 v[98:99], v[82:83], 0, s[2:3]
	s_mov_b64 s[2:3], 0x5000
	v_lshl_add_u64 v[140:141], v[24:25], 0, v[18:19]
	v_lshlrev_b64 v[18:19], 11, v[142:143]
	v_lshl_add_u64 v[100:101], v[82:83], 0, s[2:3]
	s_mov_b64 s[2:3], 0x5800
	v_lshl_add_u64 v[142:143], v[24:25], 0, v[18:19]
	v_lshlrev_b64 v[18:19], 11, v[144:145]
	v_lshl_add_u64 v[102:103], v[82:83], 0, s[2:3]
	s_mov_b64 s[2:3], 0x6000
	v_lshl_add_u64 v[144:145], v[24:25], 0, v[18:19]
	v_lshlrev_b64 v[18:19], 11, v[146:147]
	v_lshl_add_u64 v[104:105], v[82:83], 0, s[2:3]
	s_mov_b64 s[2:3], 0x6800
	v_lshl_add_u64 v[146:147], v[24:25], 0, v[18:19]
	v_lshlrev_b64 v[18:19], 11, v[148:149]
	v_lshl_add_u64 v[106:107], v[82:83], 0, s[2:3]
	s_mov_b64 s[2:3], 0x7000
	v_lshl_add_u64 v[148:149], v[24:25], 0, v[18:19]
	v_lshlrev_b64 v[18:19], 11, v[150:151]
	v_lshl_add_u64 v[108:109], v[82:83], 0, s[2:3]
	s_mov_b64 s[2:3], 0x7800
	v_lshl_add_u64 v[150:151], v[24:25], 0, v[18:19]
	v_mov_b32_e32 v18, 0
	v_lshl_add_u64 v[110:111], v[82:83], 0, s[2:3]
	v_lshl_add_u64 v[152:153], v[28:29], 0, v[72:73]
	v_lshl_add_u64 v[154:155], v[28:29], 0, v[74:75]
	v_lshl_add_u64 v[156:157], v[28:29], 0, v[76:77]
	v_lshl_add_u64 v[158:159], v[28:29], 0, v[78:79]
	s_mov_b64 s[2:3], -1
	v_mov_b32_e32 v19, v18
	v_mov_b32_e32 v20, v18
	v_mov_b32_e32 v21, v18
	v_mov_b32_e32 v26, v18
	v_mov_b32_e32 v27, v18
	v_mov_b32_e32 v28, v18
	v_mov_b32_e32 v29, v18
	v_mov_b32_e32 v22, v18
	v_mov_b32_e32 v23, v18
	v_mov_b32_e32 v24, v18
	v_mov_b32_e32 v25, v18
	v_mov_b32_e32 v30, v18
	v_mov_b32_e32 v31, v18
	v_mov_b32_e32 v32, v18
	v_mov_b32_e32 v33, v18
	s_branch .LBB0_1097

; __device__ __forceinline__ void c3_phase(LAS unsigned char* lds, const bf16_t* __restrict__ QH, const bf16_t* __restrict__ LF, const bf16_t* __restrict__ VTH, const bf16_t* __restrict__ SIN, ...
;     ...
;         for (int et = 0; et < 4; ++et) {
;             const int e0 = (eh * 4 + et) * 16 + 4 * g4;
;             const f32x4 gn = *(const f32x4*)(hg_gain + e0);
;             const u32x2 gv = *(const u32x2*)(GS + tok * 512 + h * 128 + e0);
.LBB0_1100:
	s_mov_b64 s[92:93], 0
	v_readlane_b32 vcc_lo, v254, 28
	v_readlane_b32 vcc_hi, v254, 29
	s_nop 1
	v_or_b32_e32 v246, vcc_lo, v64
	v_mov_b32_e32 v247, vcc_hi
	v_readlane_b32 vcc_lo, v254, 14
	v_readlane_b32 vcc_hi, v254, 15
	v_lshlrev_b64 v[246:247], 10, v[246:247]
	s_nop 0
	v_lshl_add_u64 v[246:247], vcc, 0, v[246:247]
	v_readlane_b32 vcc_lo, v254, 27
	s_mov_b32 vcc_hi, 0
	s_lshl_b32 vcc_lo, vcc_lo, 1
	v_lshl_add_u64 v[246:247], v[246:247], 0, v[80:81]
	s_nop 0
	v_lshl_add_u64 v[246:247], v[246:247], 0, vcc
	global_load_dwordx4 v[190:193], v[68:69], off
	global_load_dwordx4 v[194:197], v[68:69], off offset:64
	global_load_dwordx4 v[198:201], v[68:69], off offset:128
	global_load_dwordx4 v[202:205], v[68:69], off offset:192
	global_load_dwordx2 v[238:239], v[246:247], off
	global_load_dwordx2 v[240:241], v[246:247], off offset:32
	global_load_dwordx2 v[242:243], v[246:247], off offset:64
	global_load_dwordx2 v[244:245], v[246:247], off offset:96
